# speedup vs baseline: 1.0161x; 1.0120x over previous
.LBB1_12:
	s_mov_b32 s0, s44
	s_add_i32 s44, s44, 1
	s_cmp_ge_u32 s44, s42
	s_cselect_b64 s[22:23], -1, 0
	s_cmp_lt_u32 s44, s42
	s_cselect_b32 s2, s44, s0
	s_waitcnt vmcnt(0)
	s_lshl_b32 s0, s2, 4
	s_mov_b32 s1, s17
	s_mov_b32 m0, s43
	ds_read_b128 v[76:79], v119 offset:32768
	ds_read_b128 v[80:83], v119 offset:36864
	ds_read_b128 v[84:87], v120 offset:32768
	ds_read_b128 v[88:91], v120 offset:36864
	ds_read_b128 v[92:95], v121
	ds_read_b128 v[96:99], v121 offset:4096
	ds_read_b128 v[128:131], v122
	ds_read_b128 v[132:135], v122 offset:4096
	ds_read_b128 v[72:75], v123
	s_waitcnt lgkmcnt(0)
	v_lshl_add_u64 v[70:71], s[0:1], 2, v[2:3]
	global_load_lds_dword v[70:71], off
	ds_read_b128 v[156:159], v115
	ds_read_b128 v[160:163], v115 offset:1024
	ds_read_b128 v[164:167], v115 offset:2048
	v_cvt_pk_bf16_f32 v136, v76, v77
	v_cvt_pk_bf16_f32 v137, v78, v79
	v_cvt_pk_bf16_f32 v138, v84, v85
	v_cvt_pk_bf16_f32 v139, v86, v87
	v_cvt_pk_bf16_f32 v140, v92, v93
	v_cvt_pk_bf16_f32 v141, v94, v95
	v_cvt_pk_bf16_f32 v142, v128, v129
	v_cvt_pk_bf16_f32 v143, v130, v131
	v_cvt_pk_bf16_f32 v144, v80, v81
	v_cvt_pk_bf16_f32 v145, v82, v83
	v_cvt_pk_bf16_f32 v146, v88, v89
	v_cvt_pk_bf16_f32 v147, v90, v91
	v_cvt_pk_bf16_f32 v128, v96, v97
	v_cvt_pk_bf16_f32 v129, v98, v99
	v_cvt_pk_bf16_f32 v130, v132, v133
	v_cvt_pk_bf16_f32 v131, v134, v135
	s_lshl_b32 s0, s2, 13
	s_cmp_lt_u32 s44, s42
	s_cselect_b32 s0, s0, 0x1e848000
	s_mov_b32 s61, s0
	s_add_i32 s63, s44, 1
	s_cmp_eq_u32 s63, s42
	s_cselect_b32 s63, 1, 0
	ds_read_b128 v[132:135], v115 offset:3072
	s_waitcnt lgkmcnt(3)
	v_mfma_f32_16x16x32_bf16 v[148:151], v[136:139], v[156:159], v[36:39]
	ds_read_b128 v[156:159], v115 offset:4096
	s_waitcnt lgkmcnt(3)
	v_mfma_f32_16x16x32_bf16 v[152:155], v[136:139], v[160:163], v[40:43]
	ds_read_b128 v[160:163], v115 offset:5120
	s_waitcnt lgkmcnt(3)
	v_mfma_f32_16x16x32_bf16 v[96:99], v[136:139], v[164:167], v[44:47]
	ds_read_b128 v[164:167], v115 offset:6144
	s_waitcnt lgkmcnt(3)
	v_mfma_f32_16x16x32_bf16 v[92:95], v[136:139], v[132:135], v[48:51]
	ds_read_b128 v[132:135], v115 offset:7168
	s_waitcnt lgkmcnt(3)
	v_mfma_f32_16x16x32_bf16 v[88:91], v[136:139], v[156:159], v[52:55]
	ds_read_b128 v[156:159], v115 offset:8192
	s_waitcnt lgkmcnt(3)
	v_mfma_f32_16x16x32_bf16 v[84:87], v[136:139], v[160:163], v[56:59]
	ds_read_b128 v[160:163], v115 offset:9216
	s_waitcnt lgkmcnt(3)
	v_mfma_f32_16x16x32_bf16 v[80:83], v[136:139], v[164:167], v[60:63]
	ds_read_b128 v[164:167], v115 offset:10240
	s_waitcnt lgkmcnt(3)
	v_mfma_f32_16x16x32_bf16 v[76:79], v[136:139], v[132:135], v[64:67]
	ds_read_b128 v[132:135], v115 offset:11264
	s_waitcnt lgkmcnt(3)
	v_mfma_f32_16x16x32_bf16 v[148:151], v[140:143], v[156:159], v[148:151]
	ds_read_b128 v[156:159], v115 offset:12288
	s_waitcnt lgkmcnt(3)
	v_mfma_f32_16x16x32_bf16 v[152:155], v[140:143], v[160:163], v[152:155]
	ds_read_b128 v[160:163], v115 offset:13312
	s_waitcnt lgkmcnt(3)
	v_mfma_f32_16x16x32_bf16 v[96:99], v[140:143], v[164:167], v[96:99]
	ds_read_b128 v[164:167], v115 offset:14336
	s_waitcnt lgkmcnt(3)
	v_mfma_f32_16x16x32_bf16 v[92:95], v[140:143], v[132:135], v[92:95]
	ds_read_b128 v[132:135], v115 offset:15360
	s_waitcnt lgkmcnt(3)
	v_mfma_f32_16x16x32_bf16 v[88:91], v[140:143], v[156:159], v[88:91]
	ds_read_b128 v[156:159], v115 offset:16384
	s_waitcnt lgkmcnt(3)
	v_mfma_f32_16x16x32_bf16 v[84:87], v[140:143], v[160:163], v[84:87]
	ds_read_b128 v[160:163], v115 offset:17408
	s_waitcnt lgkmcnt(3)
	v_mfma_f32_16x16x32_bf16 v[80:83], v[140:143], v[164:167], v[80:83]
	ds_read_b128 v[164:167], v115 offset:18432
	s_waitcnt lgkmcnt(3)
	v_mfma_f32_16x16x32_bf16 v[76:79], v[140:143], v[132:135], v[76:79]
	ds_read_b128 v[132:135], v115 offset:19456
	s_waitcnt lgkmcnt(3)
	s_mov_b32 m0, s47
	s_nop 0
	buffer_load_dwordx4 v113, s[12:15], s61 offen nt lds
	s_cmp_eq_u32 s63, 0
	s_cbranch_scc1 .Lmain_noburst
	s_mov_b32 m0, s48
	s_or_b32 s62, s61, 0x800
	buffer_load_dwordx4 v113, s[12:15], s62 offen nt lds
	s_mov_b32 m0, s49
	s_or_b32 s62, s61, 0x1000
	buffer_load_dwordx4 v113, s[12:15], s62 offen nt lds
	s_mov_b32 m0, s50
	s_or_b32 s62, s61, 0x1800
	buffer_load_dwordx4 v113, s[12:15], s62 offen nt lds
	s_mov_b32 m0, s51
	s_or_b32 s62, s61, 0x100
	buffer_load_dwordx4 v113, s[12:15], s62 offen nt lds
	s_mov_b32 m0, s52
	s_or_b32 s62, s61, 0x900
	buffer_load_dwordx4 v113, s[12:15], s62 offen nt lds
	s_mov_b32 m0, s53
	s_or_b32 s62, s61, 0x1100
	buffer_load_dwordx4 v113, s[12:15], s62 offen nt lds
	s_mov_b32 m0, s54
	s_or_b32 s62, s61, 0x1900
	buffer_load_dwordx4 v113, s[12:15], s62 offen nt lds
.Lmain_noburst:
	v_mfma_f32_16x16x32_bf16 v[148:151], v[144:147], v[156:159], v[148:151]
	ds_read_b128 v[156:159], v115 offset:20480
	s_waitcnt lgkmcnt(3)
	v_mfma_f32_16x16x32_bf16 v[152:155], v[144:147], v[160:163], v[152:155]
	ds_read_b128 v[160:163], v115 offset:21504
	s_waitcnt lgkmcnt(3)
	v_mfma_f32_16x16x32_bf16 v[96:99], v[144:147], v[164:167], v[96:99]
	ds_read_b128 v[164:167], v115 offset:22528
	s_waitcnt lgkmcnt(3)
	v_mfma_f32_16x16x32_bf16 v[92:95], v[144:147], v[132:135], v[92:95]
	ds_read_b128 v[132:135], v115 offset:23552
	s_waitcnt lgkmcnt(3)
	v_mfma_f32_16x16x32_bf16 v[88:91], v[144:147], v[156:159], v[88:91]
	ds_read_b128 v[156:159], v115 offset:24576
	s_waitcnt lgkmcnt(3)
	v_mfma_f32_16x16x32_bf16 v[84:87], v[144:147], v[160:163], v[84:87]
	ds_read_b128 v[160:163], v115 offset:25600
	s_waitcnt lgkmcnt(3)
	v_mfma_f32_16x16x32_bf16 v[80:83], v[144:147], v[164:167], v[80:83]
	ds_read_b128 v[164:167], v115 offset:26624
	s_waitcnt lgkmcnt(3)
	v_mfma_f32_16x16x32_bf16 v[76:79], v[144:147], v[132:135], v[76:79]
	ds_read_b128 v[132:135], v115 offset:27648
	s_waitcnt lgkmcnt(3)
	v_mfma_f32_16x16x32_bf16 v[148:151], v[128:131], v[156:159], v[148:151]
	ds_read_b128 v[156:159], v115 offset:28672
	s_waitcnt lgkmcnt(3)
	v_mfma_f32_16x16x32_bf16 v[152:155], v[128:131], v[160:163], v[152:155]
	ds_read_b128 v[160:163], v115 offset:29696
	s_waitcnt lgkmcnt(3)
	v_mfma_f32_16x16x32_bf16 v[96:99], v[128:131], v[164:167], v[96:99]
	ds_read_b128 v[164:167], v115 offset:30720
	s_waitcnt lgkmcnt(3)
	v_mfma_f32_16x16x32_bf16 v[92:95], v[128:131], v[132:135], v[92:95]
	ds_read_b128 v[132:135], v115 offset:31744
	s_waitcnt lgkmcnt(3)
	v_mfma_f32_16x16x32_bf16 v[88:91], v[128:131], v[156:159], v[88:91]
	s_waitcnt lgkmcnt(2)
	v_mfma_f32_16x16x32_bf16 v[84:87], v[128:131], v[160:163], v[84:87]
	s_waitcnt lgkmcnt(1)
	v_mfma_f32_16x16x32_bf16 v[80:83], v[128:131], v[164:167], v[80:83]
	s_waitcnt lgkmcnt(0)
	v_mfma_f32_16x16x32_bf16 v[76:79], v[128:131], v[132:135], v[76:79]
	s_cmp_lg_u32 s63, 0
	s_cbranch_scc1 .Lmain_skip1
	s_mov_b32 m0, s48
	s_or_b32 s62, s61, 0x800
	buffer_load_dwordx4 v113, s[12:15], s62 offen nt lds
.Lmain_skip1:
	ds_read2_b32 v[136:137], v114 offset0:128 offset1:144
	ds_read2_b32 v[138:139], v125 offset1:16
	ds_read2_b32 v[140:141], v114 offset0:160 offset1:176
	ds_read2_b32 v[142:143], v125 offset0:32 offset1:48
	ds_read2_b32 v[144:145], v114 offset0:192 offset1:208
	ds_read2_b32 v[146:147], v125 offset0:64 offset1:80
	ds_read2_b32 v[156:157], v114 offset0:224 offset1:240
	ds_read2_b32 v[158:159], v125 offset0:96 offset1:112
	v_fma_f32 v70, v149, v149, 0
	v_fmac_f32_e32 v70, v153, v153
	v_fmac_f32_e32 v70, v97, v97
	v_fmac_f32_e32 v70, v93, v93
	v_fmac_f32_e32 v70, v89, v89
	v_fmac_f32_e32 v70, v85, v85
	v_fmac_f32_e32 v70, v81, v81
	v_fmac_f32_e32 v70, v77, v77
	v_fma_f32 v68, v148, v148, 0
	v_fmac_f32_e32 v68, v152, v152
	v_add_f32_dpp v70, v70, v70 quad_perm:[1,0,3,2] row_mask:0xf bank_mask:0xf bound_ctrl:1
	v_fmac_f32_e32 v68, v96, v96
	v_fmac_f32_e32 v68, v92, v92
	v_add_f32_dpp v70, v70, v70 quad_perm:[2,3,0,1] row_mask:0xf bank_mask:0xf bound_ctrl:1
	v_fmac_f32_e32 v68, v88, v88
	v_fmac_f32_e32 v68, v84, v84
	v_add_f32_dpp v70, v70, v70 row_half_mirror row_mask:0xf bank_mask:0xf bound_ctrl:1
	v_fmac_f32_e32 v68, v80, v80
	v_fmac_f32_e32 v68, v76, v76
	v_add_f32_dpp v70, v70, v70 row_mirror row_mask:0xf bank_mask:0xf bound_ctrl:1
	v_fmamk_f32 v70, v70, 0x3c000000, v124
	s_cmp_lg_u32 s63, 0
	s_cbranch_scc1 .Lmain_skip2
	s_mov_b32 m0, s49
	s_or_b32 s62, s61, 0x1000
	buffer_load_dwordx4 v113, s[12:15], s62 offen nt lds
.Lmain_skip2:
	v_rsq_f32_e32 v127, v70
	v_fma_f32 v70, v150, v150, 0
	v_fmac_f32_e32 v70, v154, v154
	v_fmac_f32_e32 v70, v98, v98
	v_fmac_f32_e32 v70, v94, v94
	v_fmac_f32_e32 v70, v90, v90
	v_fmac_f32_e32 v70, v86, v86
	v_fmac_f32_e32 v70, v82, v82
	v_fmac_f32_e32 v70, v78, v78
	v_add_f32_dpp v68, v68, v68 quad_perm:[1,0,3,2] row_mask:0xf bank_mask:0xf bound_ctrl:1
	v_mul_f32_e32 v131, v127, v149
	v_add_f32_dpp v70, v70, v70 quad_perm:[1,0,3,2] row_mask:0xf bank_mask:0xf bound_ctrl:1
	v_add_f32_dpp v68, v68, v68 quad_perm:[2,3,0,1] row_mask:0xf bank_mask:0xf bound_ctrl:1
	v_mul_f32_e32 v81, v127, v81
	v_add_f32_dpp v70, v70, v70 quad_perm:[2,3,0,1] row_mask:0xf bank_mask:0xf bound_ctrl:1
	v_add_f32_dpp v68, v68, v68 row_half_mirror row_mask:0xf bank_mask:0xf bound_ctrl:1
	v_cmp_gt_u32_e64 s[0:1], s55, v72
	v_add_f32_dpp v70, v70, v70 row_half_mirror row_mask:0xf bank_mask:0xf bound_ctrl:1
	v_add_f32_dpp v68, v68, v68 row_mirror row_mask:0xf bank_mask:0xf bound_ctrl:1
	v_fmamk_f32 v68, v68, 0x3c000000, v124
	v_add_f32_dpp v70, v70, v70 row_mirror row_mask:0xf bank_mask:0xf bound_ctrl:1
	v_fmamk_f32 v70, v70, 0x3c000000, v124
	v_rsq_f32_e32 v130, v70
	v_fma_f32 v70, v151, v151, 0
	v_fmac_f32_e32 v70, v155, v155
	v_fmac_f32_e32 v70, v99, v99
	v_fmac_f32_e32 v70, v95, v95
	v_fmac_f32_e32 v70, v91, v91
	v_fmac_f32_e32 v70, v87, v87
	v_fmac_f32_e32 v70, v83, v83
	v_fmac_f32_e32 v70, v79, v79
	v_rsq_f32_e32 v68, v68
	v_mul_f32_e32 v98, v130, v98
	v_add_f32_dpp v70, v70, v70 quad_perm:[1,0,3,2] row_mask:0xf bank_mask:0xf bound_ctrl:1
	v_mul_f32_e32 v90, v130, v90
	v_mul_f32_e32 v111, v68, v148
	v_add_f32_dpp v110, v70, v70 quad_perm:[2,3,0,1] row_mask:0xf bank_mask:0xf bound_ctrl:1
	s_nop 1
	v_add_f32_dpp v110, v110, v110 row_half_mirror row_mask:0xf bank_mask:0xf bound_ctrl:1
	v_mul_f32_e32 v96, v68, v96
	v_mul_f32_e32 v92, v68, v92
	v_add_f32_dpp v110, v110, v110 row_mirror row_mask:0xf bank_mask:0xf bound_ctrl:1
	v_fmamk_f32 v110, v110, 0x3c000000, v124
	s_waitcnt lgkmcnt(0)
	s_cmp_lg_u32 s63, 0
	s_cbranch_scc1 .Lmain_skip3
	s_mov_b32 m0, s50
	s_or_b32 s62, s61, 0x1800
	buffer_load_dwordx4 v113, s[12:15], s62 offen nt lds
.Lmain_skip3:
	v_fma_f32 v111, v111, v136, v138
	v_fma_f32 v131, v131, v136, v138
	v_exp_f32_e32 v111, v111
	v_exp_f32_e32 v131, v131
	v_rsq_f32_e32 v132, v110
	v_mul_f32_e32 v88, v68, v88
	v_add_f32_e32 v110, 1.0, v111
	v_add_f32_e32 v111, 1.0, v131
	v_mul_f32_e32 v131, v130, v150
	v_mul_f32_e32 v133, v132, v151
	v_fma_f32 v131, v131, v136, v138
	v_fma_f32 v70, v133, v136, v138
	v_exp_f32_e32 v131, v131
	v_exp_f32_e32 v70, v70
	v_rcp_f32_e32 v110, v110
	v_rcp_f32_e32 v111, v111
	v_add_f32_e32 v128, 1.0, v131
	v_add_f32_e32 v70, 1.0, v70
	v_rcp_f32_e32 v128, v128
	v_rcp_f32_e32 v70, v70
	v_mul_f32_e32 v131, v68, v152
	v_fma_f32 v131, v131, v137, v139
	v_cvt_pk_bf16_f32 v110, v110, v111
	v_cvt_pk_bf16_f32 v111, v128, v70
	v_mul_f32_e32 v128, v127, v153
	v_exp_f32_e32 v131, v131
	v_fma_f32 v128, v128, v137, v139
	v_exp_f32_e32 v128, v128
	v_mul_f32_e32 v99, v132, v99
	v_add_f32_e32 v70, 1.0, v131
	v_rcp_f32_e32 v133, v70
	v_add_f32_e32 v70, 1.0, v128
	v_mul_f32_e32 v131, v130, v154
	v_rcp_f32_e32 v134, v70
	v_mul_f32_e32 v70, v132, v155
	v_fma_f32 v131, v131, v137, v139
	v_fma_f32 v129, v70, v137, v139
	v_exp_f32_e32 v135, v129
	v_exp_f32_e32 v131, v131
	v_mul_f32_e32 v91, v132, v91
	v_add_f32_e32 v135, 1.0, v135
	v_rcp_f32_e32 v135, v135
	s_cmp_lg_u32 s63, 0
	s_cbranch_scc1 .Lmain_skip4
	s_mov_b32 m0, s51
	s_or_b32 s62, s61, 0x100
	buffer_load_dwordx4 v113, s[12:15], s62 offen nt lds
.Lmain_skip4:
	v_fma_f32 v96, v96, v140, v142
	v_exp_f32_e32 v136, v96
	v_mul_f32_e32 v96, v127, v97
	v_fma_f32 v96, v96, v140, v142
	v_exp_f32_e32 v97, v96
	v_fma_f32 v98, v98, v140, v142
	v_fma_f32 v70, v99, v140, v142
	v_exp_f32_e32 v98, v98
	v_exp_f32_e32 v70, v70
	v_add_f32_e32 v97, 1.0, v97
	v_cvt_pk_bf16_f32 v96, v133, v134
	v_add_f32_e32 v133, 1.0, v136
	v_rcp_f32_e32 v99, v97
	v_add_f32_e32 v97, 1.0, v98
	v_add_f32_e32 v70, 1.0, v70
	v_fma_f32 v92, v92, v141, v143
	v_rcp_f32_e32 v133, v133
	v_rcp_f32_e32 v128, v97
	v_rcp_f32_e32 v70, v70
	v_exp_f32_e32 v92, v92
	v_cvt_pk_bf16_f32 v98, v133, v99
	v_add_f32_e32 v131, 1.0, v131
	v_cvt_pk_bf16_f32 v99, v128, v70
	v_add_f32_e32 v70, 1.0, v92
	v_mul_f32_e32 v92, v127, v93
	v_fma_f32 v92, v92, v141, v143
	v_exp_f32_e32 v92, v92
	v_mul_f32_e32 v93, v130, v94
	v_fma_f32 v93, v93, v141, v143
	v_rcp_f32_e32 v131, v131
	v_exp_f32_e32 v93, v93
	v_rcp_f32_e32 v94, v70
	v_add_f32_e32 v70, 1.0, v92
	v_rcp_f32_e32 v128, v70
	v_mul_f32_e32 v70, v132, v95
	v_cvt_pk_bf16_f32 v97, v131, v135
	v_add_f32_e32 v131, 1.0, v93
	v_fma_f32 v129, v70, v141, v143
	v_exp_f32_e32 v95, v129
	v_rcp_f32_e32 v129, v131
	v_mul_f32_e32 v84, v68, v84
	v_mul_f32_e32 v80, v68, v80
	s_cmp_lg_u32 s63, 0
	s_cbranch_scc1 .Lmain_skip5
	s_mov_b32 m0, s52
	s_or_b32 s62, s61, 0x900
	buffer_load_dwordx4 v113, s[12:15], s62 offen nt lds
.Lmain_skip5:
	v_fma_f32 v88, v88, v144, v146
	v_exp_f32_e32 v131, v88
	v_mul_f32_e32 v88, v127, v89
	v_fma_f32 v88, v88, v144, v146
	v_exp_f32_e32 v89, v88
	v_fma_f32 v90, v90, v144, v146
	v_fma_f32 v70, v91, v144, v146
	v_exp_f32_e32 v90, v90
	v_exp_f32_e32 v70, v70
	v_add_f32_e32 v89, 1.0, v89
	v_cvt_pk_bf16_f32 v88, v94, v128
	v_add_f32_e32 v94, 1.0, v131
	v_rcp_f32_e32 v91, v89
	v_add_f32_e32 v89, 1.0, v90
	v_add_f32_e32 v70, 1.0, v70
	v_fma_f32 v84, v84, v145, v147
	v_rcp_f32_e32 v94, v94
	v_rcp_f32_e32 v92, v89
	v_rcp_f32_e32 v70, v70
	v_exp_f32_e32 v84, v84
	v_cvt_pk_bf16_f32 v90, v94, v91
	v_mul_f32_e32 v68, v68, v76
	v_cvt_pk_bf16_f32 v91, v92, v70
	v_add_f32_e32 v70, 1.0, v84
	v_mul_f32_e32 v84, v127, v85
	v_fma_f32 v84, v84, v145, v147
	v_mul_f32_e32 v85, v130, v86
	v_exp_f32_e32 v84, v84
	v_fma_f32 v85, v85, v145, v147
	v_exp_f32_e32 v85, v85
	v_rcp_f32_e32 v92, v70
	v_add_f32_e32 v70, 1.0, v84
	v_rcp_f32_e32 v84, v70
	v_add_f32_e32 v70, 1.0, v85
	v_mul_f32_e32 v85, v132, v87
	v_fma_f32 v93, v85, v145, v147
	v_exp_f32_e32 v85, v93
	v_rcp_f32_e32 v93, v70
	v_mul_f32_e32 v76, v127, v77
	v_mul_f32_e32 v82, v130, v82
	v_mul_f32_e32 v83, v132, v83
	v_mul_f32_e32 v77, v130, v78
	s_cmp_lg_u32 s63, 0
	s_cbranch_scc1 .Lmain_skip6
	s_mov_b32 m0, s53
	s_or_b32 s62, s61, 0x1100
	buffer_load_dwordx4 v113, s[12:15], s62 offen nt lds
.Lmain_skip6:
	v_fma_f32 v76, v76, v157, v159
	v_mul_f32_e32 v78, v132, v79
	v_fma_f32 v80, v80, v156, v158
	v_fma_f32 v81, v81, v156, v158
	v_fma_f32 v82, v82, v156, v158
	v_fma_f32 v70, v83, v156, v158
	v_fma_f32 v68, v68, v157, v159
	v_exp_f32_e32 v76, v76
	v_fma_f32 v77, v77, v157, v159
	v_fma_f32 v87, v78, v157, v159
	v_exp_f32_e32 v82, v82
	v_exp_f32_e32 v70, v70
	v_exp_f32_e32 v68, v68
	v_exp_f32_e32 v77, v77
	v_exp_f32_e32 v71, v87
	v_add_f32_e32 v76, 1.0, v76
	v_add_f32_e32 v82, 1.0, v82
	v_add_f32_e32 v70, 1.0, v70
	v_add_f32_e32 v68, 1.0, v68
	v_rcp_f32_e32 v78, v76
	v_add_f32_e32 v76, 1.0, v77
	v_add_f32_e32 v71, 1.0, v71
	v_rcp_f32_e32 v82, v82
	v_rcp_f32_e32 v70, v70
	v_rcp_f32_e32 v68, v68
	v_rcp_f32_e32 v79, v76
	v_rcp_f32_e32 v71, v71
	v_exp_f32_e32 v80, v80
	v_exp_f32_e32 v81, v81
	v_cvt_pk_bf16_f32 v77, v82, v70
	v_cvt_pk_bf16_f32 v78, v68, v78
	v_cvt_pk_bf16_f32 v79, v79, v71
	v_subrev_u32_e32 v68, s16, v72
	v_subrev_u32_e32 v70, s16, v73
	v_subrev_u32_e32 v71, s16, v74
	v_add_f32_e32 v95, 1.0, v95
	v_add_f32_e32 v85, 1.0, v85
	v_add_f32_e32 v80, 1.0, v80
	v_add_f32_e32 v81, 1.0, v81
	s_cmp_lg_u32 s63, 0
	s_cbranch_scc1 .Lmain_skip7
	s_mov_b32 m0, s54
	s_or_b32 s62, s61, 0x1900
	buffer_load_dwordx4 v113, s[12:15], s62 offen nt lds
